# v8 (batched attention ss reduction) with 192 B of unreachable padding after the epilogue so every later instruction keeps the address it has in v6
# speedup vs baseline: 1.0047x; 1.0027x over previous
.LBB0_1136:
	s_or_b64 exec, exec, s[0:1]
	s_movk_i32 s0, 0x100
	v_cmp_gt_u32_e32 vcc, s0, v165
	s_waitcnt lgkmcnt(0)
	s_barrier
	s_and_saveexec_b64 s[12:13], vcc
	s_cbranch_execz .LBB0_1116
	v_lshlrev_b32_e32 v107, 8, v165
	v_lshl_add_u32 v106, v200, 2, 0
	v_and_b32_e32 v66, 0xc000, v107
	v_add_u32_e32 v108, v106, v66
	ds_read2st64_b32 v[136:137], v108 offset1:1
	ds_read2st64_b32 v[138:139], v108 offset0:2 offset1:3
	ds_read2st64_b32 v[140:141], v108 offset0:4 offset1:5
	ds_read2st64_b32 v[142:143], v108 offset0:6 offset1:7
	ds_read2st64_b32 v[144:145], v108 offset0:8 offset1:9
	ds_read2st64_b32 v[146:147], v108 offset0:10 offset1:11
	ds_read2st64_b32 v[148:149], v108 offset0:14 offset1:15
	ds_read2st64_b32 v[150:151], v108 offset0:12 offset1:13
	ds_read2st64_b32 v[152:153], v108 offset0:18 offset1:19
	ds_read2st64_b32 v[154:155], v108 offset0:16 offset1:17
	v_lshlrev_b32_e32 v162, 2, v175
	s_lshl_b64 s[0:1], s[6:7], 11
	v_readlane_b32 s2, v251, 35
	s_add_u32 s0, s2, s0
	s_waitcnt lgkmcnt(9)
	v_fma_f32 v73, v50, v105, -v136
	v_fma_f32 v72, v51, v104, -v137
	v_readlane_b32 s2, v251, 37
	s_addc_u32 s1, s2, s1
	s_lshl_b32 s2, s39, 8
	s_add_u32 s6, s0, s2
	s_waitcnt lgkmcnt(8)
	v_fma_f32 v71, v52, v101, -v138
	v_fma_f32 v70, v53, v99, -v139
	s_addc_u32 s7, s1, 0
	v_mov_b32_e32 v165, v163
	s_movk_i32 s0, 0x1000
	s_waitcnt lgkmcnt(7)
	v_fma_f32 v69, v54, v95, -v140
	v_fma_f32 v67, v55, v102, -v141
	s_waitcnt lgkmcnt(6)
	v_fma_f32 v68, v56, v98, -v142
	v_fma_f32 v66, v57, v96, -v143
	s_waitcnt lgkmcnt(5)
	v_fma_f32 v57, v58, v103, -v144
	v_fma_f32 v56, v59, v100, -v145
	s_waitcnt lgkmcnt(4)
	v_fma_f32 v55, v60, v97, -v146
	v_fma_f32 v54, v61, v94, -v147
	s_waitcnt lgkmcnt(3)
	v_fma_f32 v52, v64, v91, -v148
	s_waitcnt lgkmcnt(2)
	v_fma_f32 v53, v62, v93, -v150
	v_fma_f32 v50, v65, v90, -v149
	v_fma_f32 v51, v63, v92, -v151
	s_waitcnt lgkmcnt(0)
	v_fma_f32 v35, v35, v104, -v155
	s_waitcnt lgkmcnt(1)
	v_fma_f32 v59, v36, v101, -v152
	v_fma_f32 v36, v37, v99, -v153
	v_fma_f32 v58, v34, v105, -v154
	ds_read2st64_b32 v[136:137], v108 offset0:26 offset1:27
	ds_read2st64_b32 v[138:139], v108 offset0:20 offset1:21
	ds_read2st64_b32 v[140:141], v108 offset0:22 offset1:23
	ds_read2st64_b32 v[142:143], v108 offset0:24 offset1:25
	ds_read2st64_b32 v[144:145], v108 offset0:28 offset1:29
	ds_read2st64_b32 v[146:147], v108 offset0:30 offset1:31
	ds_read2st64_b32 v[148:149], v108 offset0:32 offset1:33
	ds_read2st64_b32 v[150:151], v108 offset0:34 offset1:35
	ds_read2st64_b32 v[152:153], v108 offset0:36 offset1:37
	ds_read2st64_b32 v[154:155], v108 offset0:38 offset1:39
	ds_read2st64_b32 v[156:157], v108 offset0:40 offset1:41
	ds_read2st64_b32 v[158:159], v108 offset0:42 offset1:43
	ds_read2st64_b32 v[160:161], v108 offset0:46 offset1:47
	ds_read2st64_b32 v[226:227], v108 offset0:44 offset1:45
	v_mul_f32_e32 v86, v58, v58
	v_fmac_f32_e32 v86, v73, v73
	v_mul_f32_e32 v82, v35, v35
	s_waitcnt lgkmcnt(12)
	v_fma_f32 v37, v38, v95, -v138
	v_fma_f32 v34, v39, v102, -v139
	v_fmac_f32_e32 v82, v72, v72
	v_mul_f32_e32 v83, v59, v59
	v_fmac_f32_e32 v83, v71, v71
	v_mul_f32_e32 v78, v36, v36
	s_waitcnt lgkmcnt(11)
	v_fma_f32 v61, v40, v98, -v140
	v_fma_f32 v60, v41, v96, -v141
	s_waitcnt lgkmcnt(13)
	v_fma_f32 v40, v45, v94, -v137
	v_fmac_f32_e32 v78, v70, v70
	v_mul_f32_e32 v80, v37, v37
	v_fmac_f32_e32 v80, v69, v69
	s_waitcnt lgkmcnt(10)
	v_fma_f32 v41, v42, v103, -v142
	v_fma_f32 v38, v43, v100, -v143
	v_fma_f32 v43, v44, v97, -v136
	v_mul_f32_e32 v74, v34, v34
	v_fmac_f32_e32 v74, v67, v67
	v_mul_f32_e32 v89, v61, v61
	v_fmac_f32_e32 v89, v68, v68
	s_waitcnt lgkmcnt(9)
	v_fma_f32 v42, v46, v93, -v144
	v_fma_f32 v39, v47, v92, -v145
	v_mul_f32_e32 v87, v60, v60
	v_fmac_f32_e32 v87, v66, v66
	v_mul_f32_e32 v84, v41, v41
	v_fmac_f32_e32 v84, v57, v57
	s_waitcnt lgkmcnt(8)
	v_fma_f32 v45, v48, v91, -v146
	v_fma_f32 v44, v49, v90, -v147
	v_mul_f32_e32 v79, v38, v38
	v_fmac_f32_e32 v79, v56, v56
	v_mul_f32_e32 v81, v43, v43
	v_fmac_f32_e32 v81, v55, v55
	s_waitcnt lgkmcnt(7)
	v_fma_f32 v76, v18, v105, -v148
	v_fma_f32 v63, v19, v104, -v149
	v_fmac_f32_e32 v86, v76, v76
	v_fmac_f32_e32 v82, v63, v63
	v_mul_f32_e32 v75, v40, v40
	v_fmac_f32_e32 v75, v54, v54
	s_waitcnt lgkmcnt(6)
	v_fma_f32 v65, v20, v101, -v150
	v_fma_f32 v62, v21, v99, -v151
	v_fmac_f32_e32 v83, v65, v65
	v_fmac_f32_e32 v78, v62, v62
	v_mul_f32_e32 v77, v42, v42
	v_fmac_f32_e32 v77, v53, v53
	s_waitcnt lgkmcnt(5)
	v_fma_f32 v49, v22, v95, -v152
	v_fma_f32 v48, v23, v102, -v153
	v_fmac_f32_e32 v80, v49, v49
	v_fmac_f32_e32 v74, v48, v48
	v_mul_f32_e32 v64, v39, v39
	v_fmac_f32_e32 v64, v51, v51
	s_waitcnt lgkmcnt(4)
	v_fma_f32 v47, v24, v98, -v154
	v_fma_f32 v46, v25, v96, -v155
	v_fmac_f32_e32 v89, v47, v47
	v_fmac_f32_e32 v87, v46, v46
	v_mul_f32_e32 v88, v45, v45
	v_fmac_f32_e32 v88, v52, v52
	s_waitcnt lgkmcnt(3)
	v_fma_f32 v25, v26, v103, -v156
	v_fma_f32 v24, v27, v100, -v157
	v_fmac_f32_e32 v84, v25, v25
	v_fmac_f32_e32 v79, v24, v24
	v_mul_f32_e32 v85, v44, v44
	s_waitcnt lgkmcnt(2)
	v_fma_f32 v23, v28, v97, -v158
	v_fma_f32 v22, v29, v94, -v159
	v_fmac_f32_e32 v81, v23, v23
	v_fmac_f32_e32 v75, v22, v22
	v_fmac_f32_e32 v85, v50, v50
	s_waitcnt lgkmcnt(0)
	v_fma_f32 v21, v30, v93, -v226
	v_fma_f32 v20, v31, v92, -v227
	s_waitcnt lgkmcnt(1)
	v_fma_f32 v19, v32, v91, -v160
	v_fma_f32 v18, v33, v90, -v161
	ds_read2st64_b32 v[136:137], v108 offset0:48 offset1:49
	ds_read2st64_b32 v[138:139], v108 offset0:50 offset1:51
	ds_read2st64_b32 v[140:141], v108 offset0:52 offset1:53
	ds_read2st64_b32 v[142:143], v108 offset0:54 offset1:55
	ds_read2st64_b32 v[144:145], v108 offset0:56 offset1:57
	ds_read2st64_b32 v[146:147], v108 offset0:58 offset1:59
	ds_read2st64_b32 v[148:149], v108 offset0:60 offset1:61
	v_fmac_f32_e32 v77, v21, v21
	v_fmac_f32_e32 v64, v20, v20
	v_fmac_f32_e32 v88, v19, v19
	v_fmac_f32_e32 v85, v18, v18
	s_waitcnt lgkmcnt(6)
	v_fma_f32 v33, v2, v105, -v136
	v_fma_f32 v32, v3, v104, -v137
	v_fmac_f32_e32 v86, v33, v33
	v_fmac_f32_e32 v82, v32, v32
	s_waitcnt lgkmcnt(5)
	v_fma_f32 v31, v4, v101, -v138
	v_fma_f32 v30, v5, v99, -v139
	v_fmac_f32_e32 v83, v31, v31
	v_fmac_f32_e32 v78, v30, v30
	s_waitcnt lgkmcnt(4)
	v_fma_f32 v29, v6, v95, -v140
	v_fma_f32 v28, v7, v102, -v141
	v_fmac_f32_e32 v80, v29, v29
	v_fmac_f32_e32 v74, v28, v28
	s_waitcnt lgkmcnt(3)
	v_fma_f32 v27, v8, v98, -v142
	v_fma_f32 v26, v9, v96, -v143
	v_fmac_f32_e32 v89, v27, v27
	v_fmac_f32_e32 v87, v26, v26
	s_waitcnt lgkmcnt(2)
	v_fma_f32 v9, v10, v103, -v144
	v_fma_f32 v8, v11, v100, -v145
	v_fmac_f32_e32 v84, v9, v9
	v_fmac_f32_e32 v79, v8, v8
	s_waitcnt lgkmcnt(1)
	v_fma_f32 v7, v12, v97, -v146
	v_fma_f32 v6, v13, v94, -v147
	v_fmac_f32_e32 v81, v7, v7
	v_fmac_f32_e32 v75, v6, v6
	s_waitcnt lgkmcnt(0)
	v_fma_f32 v5, v14, v93, -v148
	v_fma_f32 v4, v15, v92, -v149
	v_lshl_add_u64 v[14:15], s[48:49], 0, v[162:163]
	flat_load_dword v10, v[14:15]
	flat_load_dword v11, v[14:15] offset:128
	flat_load_dword v12, v[14:15] offset:256
	flat_load_dword v13, v[14:15] offset:384
	v_and_b32_e32 v15, 64, v189
	ds_read_b32 v2, v108 offset:15872
	v_xor_b32_e32 v14, 16, v189
	v_add_u32_e32 v15, 64, v15
	v_cmp_lt_i32_e32 vcc, v14, v15
	v_fmac_f32_e32 v77, v5, v5
	v_cndmask_b32_e32 v14, v189, v14, vcc
	v_lshlrev_b32_e32 v14, 2, v14
	s_waitcnt lgkmcnt(0)
	v_fma_f32 v3, v16, v91, -v2
	v_fmac_f32_e32 v64, v4, v4
	v_fmac_f32_e32 v88, v3, v3
	v_or_b32_e32 v2, 0x3f00, v107
	v_add_u32_e32 v2, v106, v2
	ds_read_b32 v2, v2
	v_lshlrev_b32_e32 v162, 1, v175
	s_waitcnt lgkmcnt(0)
	v_fma_f32 v2, v17, v90, -v2
	v_fmac_f32_e32 v85, v2, v2
	v_add_f32_dpp v86, v86, v86 quad_perm:[1,0,3,2] row_mask:0xf bank_mask:0xf bound_ctrl:1
	v_add_f32_dpp v82, v82, v82 quad_perm:[1,0,3,2] row_mask:0xf bank_mask:0xf bound_ctrl:1
	v_add_f32_dpp v83, v83, v83 quad_perm:[1,0,3,2] row_mask:0xf bank_mask:0xf bound_ctrl:1
	v_add_f32_dpp v78, v78, v78 quad_perm:[1,0,3,2] row_mask:0xf bank_mask:0xf bound_ctrl:1
	v_add_f32_dpp v80, v80, v80 quad_perm:[1,0,3,2] row_mask:0xf bank_mask:0xf bound_ctrl:1
	v_add_f32_dpp v74, v74, v74 quad_perm:[1,0,3,2] row_mask:0xf bank_mask:0xf bound_ctrl:1
	v_add_f32_dpp v89, v89, v89 quad_perm:[1,0,3,2] row_mask:0xf bank_mask:0xf bound_ctrl:1
	v_add_f32_dpp v87, v87, v87 quad_perm:[1,0,3,2] row_mask:0xf bank_mask:0xf bound_ctrl:1
	v_add_f32_dpp v84, v84, v84 quad_perm:[1,0,3,2] row_mask:0xf bank_mask:0xf bound_ctrl:1
	v_add_f32_dpp v79, v79, v79 quad_perm:[1,0,3,2] row_mask:0xf bank_mask:0xf bound_ctrl:1
	v_add_f32_dpp v81, v81, v81 quad_perm:[1,0,3,2] row_mask:0xf bank_mask:0xf bound_ctrl:1
	v_add_f32_dpp v75, v75, v75 quad_perm:[1,0,3,2] row_mask:0xf bank_mask:0xf bound_ctrl:1
	v_add_f32_dpp v77, v77, v77 quad_perm:[1,0,3,2] row_mask:0xf bank_mask:0xf bound_ctrl:1
	v_add_f32_dpp v64, v64, v64 quad_perm:[1,0,3,2] row_mask:0xf bank_mask:0xf bound_ctrl:1
	v_add_f32_dpp v88, v88, v88 quad_perm:[1,0,3,2] row_mask:0xf bank_mask:0xf bound_ctrl:1
	v_add_f32_dpp v85, v85, v85 quad_perm:[1,0,3,2] row_mask:0xf bank_mask:0xf bound_ctrl:1
	v_add_f32_dpp v86, v86, v86 quad_perm:[2,3,0,1] row_mask:0xf bank_mask:0xf bound_ctrl:1
	v_add_f32_dpp v82, v82, v82 quad_perm:[2,3,0,1] row_mask:0xf bank_mask:0xf bound_ctrl:1
	v_add_f32_dpp v83, v83, v83 quad_perm:[2,3,0,1] row_mask:0xf bank_mask:0xf bound_ctrl:1
	v_add_f32_dpp v78, v78, v78 quad_perm:[2,3,0,1] row_mask:0xf bank_mask:0xf bound_ctrl:1
	v_add_f32_dpp v80, v80, v80 quad_perm:[2,3,0,1] row_mask:0xf bank_mask:0xf bound_ctrl:1
	v_add_f32_dpp v74, v74, v74 quad_perm:[2,3,0,1] row_mask:0xf bank_mask:0xf bound_ctrl:1
	v_add_f32_dpp v89, v89, v89 quad_perm:[2,3,0,1] row_mask:0xf bank_mask:0xf bound_ctrl:1
	v_add_f32_dpp v87, v87, v87 quad_perm:[2,3,0,1] row_mask:0xf bank_mask:0xf bound_ctrl:1
	v_add_f32_dpp v84, v84, v84 quad_perm:[2,3,0,1] row_mask:0xf bank_mask:0xf bound_ctrl:1
	v_add_f32_dpp v79, v79, v79 quad_perm:[2,3,0,1] row_mask:0xf bank_mask:0xf bound_ctrl:1
	v_add_f32_dpp v81, v81, v81 quad_perm:[2,3,0,1] row_mask:0xf bank_mask:0xf bound_ctrl:1
	v_add_f32_dpp v75, v75, v75 quad_perm:[2,3,0,1] row_mask:0xf bank_mask:0xf bound_ctrl:1
	v_add_f32_dpp v77, v77, v77 quad_perm:[2,3,0,1] row_mask:0xf bank_mask:0xf bound_ctrl:1
	v_add_f32_dpp v64, v64, v64 quad_perm:[2,3,0,1] row_mask:0xf bank_mask:0xf bound_ctrl:1
	v_add_f32_dpp v88, v88, v88 quad_perm:[2,3,0,1] row_mask:0xf bank_mask:0xf bound_ctrl:1
	v_add_f32_dpp v85, v85, v85 quad_perm:[2,3,0,1] row_mask:0xf bank_mask:0xf bound_ctrl:1
	v_add_f32_dpp v86, v86, v86 row_half_mirror row_mask:0xf bank_mask:0xf bound_ctrl:1
	v_add_f32_dpp v82, v82, v82 row_half_mirror row_mask:0xf bank_mask:0xf bound_ctrl:1
	v_add_f32_dpp v83, v83, v83 row_half_mirror row_mask:0xf bank_mask:0xf bound_ctrl:1
	v_add_f32_dpp v78, v78, v78 row_half_mirror row_mask:0xf bank_mask:0xf bound_ctrl:1
	v_add_f32_dpp v80, v80, v80 row_half_mirror row_mask:0xf bank_mask:0xf bound_ctrl:1
	v_add_f32_dpp v74, v74, v74 row_half_mirror row_mask:0xf bank_mask:0xf bound_ctrl:1
	v_add_f32_dpp v89, v89, v89 row_half_mirror row_mask:0xf bank_mask:0xf bound_ctrl:1
	v_add_f32_dpp v87, v87, v87 row_half_mirror row_mask:0xf bank_mask:0xf bound_ctrl:1
	v_add_f32_dpp v84, v84, v84 row_half_mirror row_mask:0xf bank_mask:0xf bound_ctrl:1
	v_add_f32_dpp v79, v79, v79 row_half_mirror row_mask:0xf bank_mask:0xf bound_ctrl:1
	v_add_f32_dpp v81, v81, v81 row_half_mirror row_mask:0xf bank_mask:0xf bound_ctrl:1
	v_add_f32_dpp v75, v75, v75 row_half_mirror row_mask:0xf bank_mask:0xf bound_ctrl:1
	v_add_f32_dpp v77, v77, v77 row_half_mirror row_mask:0xf bank_mask:0xf bound_ctrl:1
	v_add_f32_dpp v64, v64, v64 row_half_mirror row_mask:0xf bank_mask:0xf bound_ctrl:1
	v_add_f32_dpp v88, v88, v88 row_half_mirror row_mask:0xf bank_mask:0xf bound_ctrl:1
	v_add_f32_dpp v85, v85, v85 row_half_mirror row_mask:0xf bank_mask:0xf bound_ctrl:1
	v_add_f32_dpp v86, v86, v86 row_mirror row_mask:0xf bank_mask:0xf bound_ctrl:1
	v_add_f32_dpp v82, v82, v82 row_mirror row_mask:0xf bank_mask:0xf bound_ctrl:1
	v_add_f32_dpp v83, v83, v83 row_mirror row_mask:0xf bank_mask:0xf bound_ctrl:1
	v_add_f32_dpp v78, v78, v78 row_mirror row_mask:0xf bank_mask:0xf bound_ctrl:1
	v_add_f32_dpp v80, v80, v80 row_mirror row_mask:0xf bank_mask:0xf bound_ctrl:1
	v_add_f32_dpp v74, v74, v74 row_mirror row_mask:0xf bank_mask:0xf bound_ctrl:1
	v_add_f32_dpp v89, v89, v89 row_mirror row_mask:0xf bank_mask:0xf bound_ctrl:1
	v_add_f32_dpp v87, v87, v87 row_mirror row_mask:0xf bank_mask:0xf bound_ctrl:1
	v_add_f32_dpp v84, v84, v84 row_mirror row_mask:0xf bank_mask:0xf bound_ctrl:1
	v_add_f32_dpp v79, v79, v79 row_mirror row_mask:0xf bank_mask:0xf bound_ctrl:1
	v_add_f32_dpp v81, v81, v81 row_mirror row_mask:0xf bank_mask:0xf bound_ctrl:1
	v_add_f32_dpp v75, v75, v75 row_mirror row_mask:0xf bank_mask:0xf bound_ctrl:1
	v_add_f32_dpp v77, v77, v77 row_mirror row_mask:0xf bank_mask:0xf bound_ctrl:1
	v_add_f32_dpp v64, v64, v64 row_mirror row_mask:0xf bank_mask:0xf bound_ctrl:1
	v_add_f32_dpp v88, v88, v88 row_mirror row_mask:0xf bank_mask:0xf bound_ctrl:1
	v_add_f32_dpp v85, v85, v85 row_mirror row_mask:0xf bank_mask:0xf bound_ctrl:1
	ds_bpermute_b32 v140, v14, v86
	ds_bpermute_b32 v141, v14, v82
	ds_bpermute_b32 v142, v14, v83
	ds_bpermute_b32 v143, v14, v78
	ds_bpermute_b32 v144, v14, v80
	ds_bpermute_b32 v145, v14, v74
	ds_bpermute_b32 v146, v14, v89
	ds_bpermute_b32 v147, v14, v87
	s_waitcnt lgkmcnt(0)
	v_add_f32_e32 v86, v86, v140
	v_add_f32_e32 v82, v82, v141
	v_add_f32_e32 v83, v83, v142
	v_add_f32_e32 v78, v78, v143
	v_add_f32_e32 v80, v80, v144
	v_add_f32_e32 v74, v74, v145
	v_add_f32_e32 v89, v89, v146
	v_add_f32_e32 v87, v87, v147
	v_fmamk_f32 v86, v86, 0x3c000000, v1
	v_fmamk_f32 v82, v82, 0x3c000000, v1
	v_fmamk_f32 v83, v83, 0x3c000000, v1
	v_fmamk_f32 v78, v78, 0x3c000000, v1
	v_fmamk_f32 v80, v80, 0x3c000000, v1
	v_fmamk_f32 v74, v74, 0x3c000000, v1
	v_fmamk_f32 v89, v89, 0x3c000000, v1
	v_fmamk_f32 v87, v87, 0x3c000000, v1
	v_rsq_f32_e32 v86, v86
	v_rsq_f32_e32 v82, v82
	v_rsq_f32_e32 v83, v83
	v_rsq_f32_e32 v78, v78
	v_rsq_f32_e32 v80, v80
	v_rsq_f32_e32 v74, v74
	v_rsq_f32_e32 v89, v89
	v_rsq_f32_e32 v87, v87
	ds_bpermute_b32 v140, v14, v84
	ds_bpermute_b32 v141, v14, v79
	ds_bpermute_b32 v142, v14, v81
	ds_bpermute_b32 v143, v14, v75
	ds_bpermute_b32 v144, v14, v77
	ds_bpermute_b32 v145, v14, v64
	ds_bpermute_b32 v146, v14, v88
	ds_bpermute_b32 v147, v14, v85
	s_waitcnt lgkmcnt(0)
	v_add_f32_e32 v84, v84, v140
	v_add_f32_e32 v79, v79, v141
	v_add_f32_e32 v81, v81, v142
	v_add_f32_e32 v75, v75, v143
	v_add_f32_e32 v77, v77, v144
	v_add_f32_e32 v64, v64, v145
	v_add_f32_e32 v88, v88, v146
	v_add_f32_e32 v85, v85, v147
	v_fmamk_f32 v84, v84, 0x3c000000, v1
	v_fmamk_f32 v79, v79, 0x3c000000, v1
	v_fmamk_f32 v81, v81, 0x3c000000, v1
	v_fmamk_f32 v75, v75, 0x3c000000, v1
	v_fmamk_f32 v77, v77, 0x3c000000, v1
	v_fmamk_f32 v64, v64, 0x3c000000, v1
	v_fmamk_f32 v88, v88, 0x3c000000, v1
	v_fmamk_f32 v85, v85, 0x3c000000, v1
	v_rsq_f32_e32 v84, v84
	v_rsq_f32_e32 v79, v79
	v_rsq_f32_e32 v81, v81
	v_rsq_f32_e32 v75, v75
	v_rsq_f32_e32 v77, v77
	v_rsq_f32_e32 v64, v64
	v_rsq_f32_e32 v88, v88
	v_rsq_f32_e32 v85, v85
	s_nop 0
	v_mov_b32_e32 v17, v163
	s_waitcnt vmcnt(0)
	v_mul_f32_e32 v10, v174, v10
	v_mul_f32_e32 v11, v174, v11
	v_mul_f32_e32 v12, v174, v12
	v_mul_f32_e32 v13, v174, v13
	v_mul_f32_e32 v31, v31, v83
	v_mul_f32_e32 v31, v13, v31
	v_add_u32_e32 v31, 0x8000, v31
	v_mul_f32_e32 v30, v30, v78
	v_mul_f32_e32 v30, v13, v30
	v_add_u32_e32 v30, 0x8000, v30
	v_mul_f32_e32 v29, v29, v80
	v_mul_f32_e32 v29, v13, v29
	v_add_u32_e32 v29, 0x8000, v29
	v_mul_f32_e32 v28, v28, v74
	v_mul_f32_e32 v28, v13, v28
	v_add_u32_e32 v28, 0x8000, v28
	v_mul_f32_e32 v9, v9, v84
	v_mul_f32_e32 v9, v13, v9
	v_add_u32_e32 v9, 0x8000, v9
	v_mul_f32_e32 v25, v25, v84
	v_mul_f32_e32 v25, v12, v25
	v_add_u32_e32 v25, 0x8000, v25
	v_mul_f32_e32 v8, v8, v79
	v_mul_f32_e32 v8, v13, v8
	v_add_u32_e32 v8, 0x8000, v8
	v_mul_f32_e32 v7, v7, v81
	v_mul_f32_e32 v7, v13, v7
	v_add_u32_e32 v7, 0x8000, v7
	v_mul_f32_e32 v6, v6, v75
	v_mul_f32_e32 v6, v13, v6
	v_add_u32_e32 v6, 0x8000, v6
	v_mul_f32_e32 v5, v5, v77
	v_mul_f32_e32 v5, v13, v5
	v_add_u32_e32 v5, 0x8000, v5
	v_mul_f32_e32 v4, v4, v64
	v_mul_f32_e32 v4, v13, v4
	v_add_u32_e32 v4, 0x8000, v4
	v_lshlrev_b32_e32 v16, 13, v176
	v_mul_f32_e32 v3, v3, v88
	v_mul_f32_e32 v3, v13, v3
	v_add_u32_e32 v3, 0x8000, v3
	v_lshl_add_u64 v[14:15], s[6:7], 0, v[164:165]
	v_lshl_add_u64 v[14:15], v[14:15], 0, v[162:163]
	v_lshl_add_u64 v[14:15], v[14:15], 0, v[16:17]
	v_mul_f32_e32 v16, v73, v86
	v_mul_f32_e32 v16, v10, v16
	v_add_u32_e32 v16, 0x8000, v16
	global_store_short_d16_hi v[14:15], v16, off
	v_mul_f32_e32 v16, v58, v86
	v_mul_f32_e32 v16, v11, v16
	v_add_u32_e32 v16, 0x8000, v16
	global_store_short_d16_hi v[14:15], v16, off offset:64
	v_mul_f32_e32 v16, v76, v86
	v_mul_f32_e32 v16, v12, v16
	v_add_u32_e32 v16, 0x8000, v16
	global_store_short_d16_hi v[14:15], v16, off offset:128
	v_mul_f32_e32 v16, v33, v86
	v_mul_f32_e32 v16, v13, v16
	v_add_u32_e32 v16, 0x8000, v16
	global_store_short_d16_hi v[14:15], v16, off offset:192
	v_mul_f32_e32 v16, v72, v82
	v_mul_f32_e32 v16, v10, v16
	v_add_u32_e32 v16, 0x8000, v16
	global_store_short_d16_hi v[14:15], v16, off offset:2048
	v_mul_f32_e32 v16, v35, v82
	v_mul_f32_e32 v16, v11, v16
	v_add_u32_e32 v16, 0x8000, v16
	global_store_short_d16_hi v[14:15], v16, off offset:2112
	v_mul_f32_e32 v16, v63, v82
	v_mul_f32_e32 v16, v12, v16
	v_add_u32_e32 v16, 0x8000, v16
	global_store_short_d16_hi v[14:15], v16, off offset:2176
	v_mul_f32_e32 v16, v32, v82
	v_mul_f32_e32 v16, v13, v16
	v_add_u32_e32 v16, 0x8000, v16
	global_store_short_d16_hi v[14:15], v16, off offset:2240
	v_mul_f32_e32 v16, v71, v83
	v_mul_f32_e32 v16, v10, v16
	v_add_u32_e32 v32, 0x8000, v16
	v_add_co_u32_e32 v16, vcc, s0, v14
	s_movk_i32 s0, 0x5000
	s_nop 0
	v_addc_co_u32_e32 v17, vcc, 0, v15, vcc
	global_store_short_d16_hi v[16:17], v31, off offset:192
	v_mul_f32_e32 v31, v70, v78
	v_mul_f32_e32 v31, v10, v31
	v_add_u32_e32 v31, 0x8000, v31
	global_store_short_d16_hi v[16:17], v32, off
	v_mul_f32_e32 v32, v59, v83
	global_store_short_d16_hi v[16:17], v31, off offset:2048
	v_mul_f32_e32 v31, v36, v78
	v_mul_f32_e32 v32, v11, v32
	v_mul_f32_e32 v31, v11, v31
	v_add_u32_e32 v32, 0x8000, v32
	v_add_u32_e32 v31, 0x8000, v31
	global_store_short_d16_hi v[16:17], v32, off offset:64
	v_mul_f32_e32 v32, v65, v83
	global_store_short_d16_hi v[16:17], v31, off offset:2112
	v_mul_f32_e32 v31, v62, v78
	v_mul_f32_e32 v32, v12, v32
	v_mul_f32_e32 v31, v12, v31
	v_add_u32_e32 v32, 0x8000, v32
	v_add_u32_e32 v31, 0x8000, v31
	global_store_short_d16_hi v[16:17], v32, off offset:128
	global_store_short_d16_hi v[16:17], v31, off offset:2176
	global_store_short_d16_hi v[16:17], v30, off offset:2240
	v_mul_f32_e32 v16, v69, v80
	v_mul_f32_e32 v16, v10, v16
	v_add_u32_e32 v32, 0x8000, v16
	v_add_co_u32_e32 v16, vcc, s83, v14
	v_mul_f32_e32 v2, v2, v85
	s_nop 0
	v_addc_co_u32_e32 v17, vcc, 0, v15, vcc
	global_store_short_d16_hi v[16:17], v29, off offset:192
	v_mul_f32_e32 v29, v67, v74
	v_add_co_u32_e32 v30, vcc, s0, v14
	v_mul_f32_e32 v29, v10, v29
	s_nop 0
	v_addc_co_u32_e32 v31, vcc, 0, v15, vcc
	v_add_u32_e32 v29, 0x8000, v29
	global_store_short_d16_hi v[30:31], v32, off offset:-4096
	v_mul_f32_e32 v32, v37, v80
	global_store_short_d16_hi v[16:17], v29, off offset:2048
	v_mul_f32_e32 v29, v34, v74
	v_mul_f32_e32 v32, v11, v32
	v_mul_f32_e32 v29, v11, v29
	v_add_u32_e32 v32, 0x8000, v32
	v_add_u32_e32 v29, 0x8000, v29
	global_store_short_d16_hi v[16:17], v32, off offset:64
	v_mul_f32_e32 v32, v49, v80
	global_store_short_d16_hi v[16:17], v29, off offset:2112
	v_mul_f32_e32 v29, v48, v74
	v_mul_f32_e32 v32, v12, v32
	v_mul_f32_e32 v29, v12, v29
	v_add_u32_e32 v32, 0x8000, v32
	v_add_u32_e32 v29, 0x8000, v29
	global_store_short_d16_hi v[16:17], v32, off offset:128
	global_store_short_d16_hi v[16:17], v29, off offset:2176
	global_store_short_d16_hi v[16:17], v28, off offset:2240
	v_mul_f32_e32 v16, v68, v89
	v_mul_f32_e32 v16, v10, v16
	v_add_u32_e32 v16, 0x8000, v16
	global_store_short_d16_hi v[30:31], v16, off
	v_mul_f32_e32 v16, v61, v89
	v_mul_f32_e32 v16, v11, v16
	v_add_u32_e32 v16, 0x8000, v16
	global_store_short_d16_hi v[30:31], v16, off offset:64
	v_mul_f32_e32 v16, v47, v89
	v_mul_f32_e32 v16, v12, v16
	v_add_u32_e32 v16, 0x8000, v16
	global_store_short_d16_hi v[30:31], v16, off offset:128
	v_mul_f32_e32 v16, v27, v89
	v_mul_f32_e32 v16, v13, v16
	v_add_u32_e32 v16, 0x8000, v16
	global_store_short_d16_hi v[30:31], v16, off offset:192
	v_mul_f32_e32 v16, v66, v87
	v_mul_f32_e32 v16, v10, v16
	v_add_u32_e32 v16, 0x8000, v16
	global_store_short_d16_hi v[30:31], v16, off offset:2048
	v_mul_f32_e32 v16, v60, v87
	v_mul_f32_e32 v16, v11, v16
	v_add_u32_e32 v16, 0x8000, v16
	global_store_short_d16_hi v[30:31], v16, off offset:2112
	v_mul_f32_e32 v16, v46, v87
	v_mul_f32_e32 v16, v12, v16
	v_add_u32_e32 v16, 0x8000, v16
	global_store_short_d16_hi v[30:31], v16, off offset:2176
	v_mul_f32_e32 v16, v26, v87
	v_mul_f32_e32 v16, v13, v16
	v_add_u32_e32 v16, 0x8000, v16
	global_store_short_d16_hi v[30:31], v16, off offset:2240
	v_mul_f32_e32 v16, v57, v84
	v_mul_f32_e32 v16, v10, v16
	v_add_u32_e32 v28, 0x8000, v16
	v_add_co_u32_e32 v16, vcc, s90, v14
	s_mov_b32 s0, 0x9000
	s_nop 0
	v_addc_co_u32_e32 v17, vcc, 0, v15, vcc
	v_add_co_u32_e32 v26, vcc, s0, v14
	global_store_short_d16_hi v[16:17], v9, off offset:192
	s_nop 0
	v_addc_co_u32_e32 v27, vcc, 0, v15, vcc
	v_mul_f32_e32 v9, v56, v79
	v_mul_f32_e32 v9, v10, v9
	global_store_short_d16_hi v[26:27], v7, off offset:192
	v_mul_f32_e32 v7, v54, v75
	v_add_u32_e32 v9, 0x8000, v9
	global_store_short_d16_hi v[16:17], v8, off offset:2240
	v_mul_f32_e32 v8, v55, v81
	v_mul_f32_e32 v7, v10, v7
	global_store_short_d16_hi v[16:17], v9, off offset:2048
	v_mul_f32_e32 v9, v38, v79
	v_mul_f32_e32 v8, v10, v8
	v_add_u32_e32 v7, 0x8000, v7
	v_mul_f32_e32 v9, v11, v9
	v_add_u32_e32 v8, 0x8000, v8
	global_store_short_d16_hi v[26:27], v7, off offset:2048
	v_mul_f32_e32 v7, v40, v75
	v_add_u32_e32 v9, 0x8000, v9
	global_store_short_d16_hi v[26:27], v8, off
	v_mul_f32_e32 v8, v43, v81
	v_mul_f32_e32 v7, v11, v7
	global_store_short_d16_hi v[26:27], v28, off offset:-4096
	v_mul_f32_e32 v28, v41, v84
	global_store_short_d16_hi v[16:17], v9, off offset:2112
	v_mul_f32_e32 v9, v24, v79
	v_mul_f32_e32 v8, v11, v8
	v_add_u32_e32 v7, 0x8000, v7
	v_mul_f32_e32 v28, v11, v28
	v_mul_f32_e32 v9, v12, v9
	v_add_u32_e32 v8, 0x8000, v8
	global_store_short_d16_hi v[26:27], v7, off offset:2112
	v_mul_f32_e32 v7, v22, v75
	global_store_short_d16_hi v[26:27], v6, off offset:2240
	v_mul_f32_e32 v6, v53, v77
	v_add_u32_e32 v28, 0x8000, v28
	v_add_u32_e32 v9, 0x8000, v9
	global_store_short_d16_hi v[26:27], v8, off offset:64
	v_mul_f32_e32 v8, v23, v81
	v_mul_f32_e32 v7, v12, v7
	v_mul_f32_e32 v6, v10, v6
	global_store_short_d16_hi v[16:17], v28, off offset:64
	global_store_short_d16_hi v[16:17], v25, off offset:128
	global_store_short_d16_hi v[16:17], v9, off offset:2176
	v_mul_f32_e32 v8, v12, v8
	v_add_u32_e32 v7, 0x8000, v7
	v_add_u32_e32 v16, 0x8000, v6
	v_add_co_u32_e32 v6, vcc, s16, v14
	v_add_u32_e32 v8, 0x8000, v8
	global_store_short_d16_hi v[26:27], v7, off offset:2176
	v_addc_co_u32_e32 v7, vcc, 0, v15, vcc
	s_mov_b32 s0, 0xd000
	global_store_short_d16_hi v[26:27], v8, off offset:128
	v_add_co_u32_e32 v8, vcc, s0, v14
	global_store_short_d16_hi v[6:7], v5, off offset:192
	s_nop 0
	v_addc_co_u32_e32 v9, vcc, 0, v15, vcc
	v_mul_f32_e32 v5, v51, v64
	global_store_short_d16_hi v[6:7], v4, off offset:2240
	v_mul_f32_e32 v4, v52, v88
	global_store_short_d16_hi v[8:9], v3, off offset:192
	v_mul_f32_e32 v3, v50, v85
	v_mul_f32_e32 v5, v10, v5
	v_mul_f32_e32 v4, v10, v4
	v_mul_f32_e32 v3, v10, v3
	v_add_u32_e32 v5, 0x8000, v5
	v_add_u32_e32 v4, 0x8000, v4
	v_add_u32_e32 v3, 0x8000, v3
	v_mul_f32_e32 v14, v42, v77
	global_store_short_d16_hi v[6:7], v5, off offset:2048
	v_mul_f32_e32 v5, v39, v64
	global_store_short_d16_hi v[8:9], v4, off
	v_mul_f32_e32 v4, v45, v88
	global_store_short_d16_hi v[8:9], v3, off offset:2048
	v_mul_f32_e32 v3, v44, v85
	v_mul_f32_e32 v14, v11, v14
	v_mul_f32_e32 v5, v11, v5
	v_mul_f32_e32 v4, v11, v4
	v_mul_f32_e32 v3, v11, v3
	v_add_u32_e32 v14, 0x8000, v14
	v_add_u32_e32 v5, 0x8000, v5
	v_add_u32_e32 v4, 0x8000, v4
	v_add_u32_e32 v3, 0x8000, v3
	global_store_short_d16_hi v[6:7], v14, off offset:64
	v_mul_f32_e32 v14, v21, v77
	global_store_short_d16_hi v[6:7], v5, off offset:2112
	v_mul_f32_e32 v5, v20, v64
	global_store_short_d16_hi v[8:9], v4, off offset:64
	v_mul_f32_e32 v4, v19, v88
	global_store_short_d16_hi v[8:9], v3, off offset:2112
	v_mul_f32_e32 v3, v18, v85
	v_mul_f32_e32 v14, v12, v14
	v_mul_f32_e32 v5, v12, v5
	v_mul_f32_e32 v4, v12, v4
	v_mul_f32_e32 v3, v12, v3
	v_mul_f32_e32 v2, v13, v2
	v_add_u32_e32 v14, 0x8000, v14
	v_add_u32_e32 v5, 0x8000, v5
	v_add_u32_e32 v4, 0x8000, v4
	v_add_u32_e32 v3, 0x8000, v3
	v_add_u32_e32 v2, 0x8000, v2
	global_store_short_d16_hi v[8:9], v16, off offset:-4096
	global_store_short_d16_hi v[6:7], v14, off offset:128
	global_store_short_d16_hi v[6:7], v5, off offset:2176
	global_store_short_d16_hi v[8:9], v4, off offset:128
	global_store_short_d16_hi v[8:9], v3, off offset:2176
	global_store_short_d16_hi v[8:9], v2, off offset:2240
	s_branch .LBB0_1116
	s_nop 0
	s_nop 0
	s_nop 0
	s_nop 0
	s_nop 0
	s_nop 0
	s_nop 0
	s_nop 0
	s_nop 0
	s_nop 0
	s_nop 0
	s_nop 0
	s_nop 0
	s_nop 0
	s_nop 0
	s_nop 0
	s_nop 0
	s_nop 0
	s_nop 0
	s_nop 0
	s_nop 0
	s_nop 0
	s_nop 0
	s_nop 0
	s_nop 0
	s_nop 0
	s_nop 0
	s_nop 0
	s_nop 0
	s_nop 0
	s_nop 0
	s_nop 0
	s_nop 0
	s_nop 0
	s_nop 0
	s_nop 0
	s_nop 0
	s_nop 0
	s_nop 0
	s_nop 0
	s_nop 0
	s_nop 0
	s_nop 0
	s_nop 0
	s_nop 0
	s_nop 0
	s_nop 0
	s_nop 0
